# prologue de-serialisation: phase I and phase F vector staging loops unrolled, eleven loads in flight, LDS writes as they arrive
# speedup vs baseline: 1.1907x; 1.0036x over previous
.LBB0_783:
	s_and_b64 vcc, exec, s[0:1]
	s_cbranch_vccz .LBB0_815
	v_readlane_b32 s0, v255, 1
	v_readlane_b32 s1, v255, 2
	s_lshl_b32 s28, s0, 7
	s_lshl_b64 s[0:1], s[28:29], 2
	s_add_u32 s0, s2, s0
	s_addc_u32 s1, s3, s1
	s_add_u32 s0, s0, 0x10000
	s_addc_u32 s1, s1, 0
	s_cmp_gt_i32 s44, 31
	s_mov_b64 s[6:7], -1
	s_cbranch_scc0 .LBB0_804
	s_movk_i32 s6, 0x1600
	v_cmp_gt_i32_e32 vcc, s6, v99
	s_and_saveexec_b64 s[6:7], vcc
	s_cbranch_execz .LBB0_792
	v_readlane_b32 s10, v255, 1
	v_readlane_b32 s11, v255, 2
	s_mov_b32 s12, s10
	s_mov_b32 s11, s29
	v_writelane_b32 v255, s12, 1
	s_lshl_b64 s[8:9], s[10:11], 13
	s_mul_hi_u32 s11, s10, 3
	v_writelane_b32 v255, s13, 2
	s_mul_i32 s10, s10, 3
	v_lshl_add_u32 v2, v99, 4, v98
	v_lshlrev_b32_e32 v3, 2, v99
	s_mov_b64 s[12:13], 0
	v_mov_b32_e32 v4, v99
.Lstf_0_788:
	s_movk_i32 s14, 0x11ff
	v_cmp_lt_i32_e32 vcc, s14, v4
	s_and_saveexec_b64 s[14:15], vcc
	s_xor_b64 s[14:15], exec, s[14:15]
	s_cbranch_execz .Lstf_0_790
	v_readlane_b32 s52, v253, 58
	v_and_b32_e32 v0, 0x7ffffe00, v4
	v_readlane_b32 s57, v253, 63
	v_readlane_b32 s59, v254, 1
	s_movk_i32 s18, 0x1200
	v_readlane_b32 s56, v253, 62
	v_readlane_b32 s58, v254, 0
	v_mov_b32_e32 v1, s59
	v_mov_b32_e32 v5, s57
	v_cmp_eq_u32_e32 vcc, s18, v0
	v_mov_b32_e32 v0, s58
	v_readlane_b32 s53, v253, 59
	v_cndmask_b32_e32 v1, v1, v5, vcc
	v_mov_b32_e32 v5, s56
	v_cndmask_b32_e32 v0, v0, v5, vcc
	v_readlane_b32 s54, v253, 60
	v_readlane_b32 s55, v253, 61
	v_readlane_b32 s60, v254, 2
	v_readlane_b32 s61, v254, 3
	v_readlane_b32 s62, v254, 4
	v_readlane_b32 s63, v254, 5
	v_readlane_b32 s64, v254, 6
	v_readlane_b32 s65, v254, 7
	v_readlane_b32 s66, v254, 8
	v_readlane_b32 s67, v254, 9
	v_lshl_add_u64 v[0:1], v[0:1], 0, s[8:9]

.Lstf_0_787:
	s_or_b64 exec, exec, s[14:15]
	v_mul_i32_i24_e32 v10, 0x200, v5
	v_lshlrev_b32_e32 v6, 2, v10
	v_sub_u32_e32 v6, v3, v6
	v_ashrrev_i32_e32 v7, 31, v6
	v_lshl_add_u64 v[0:1], v[6:7], 2, v[0:1]
	global_load_dwordx4 v[110:113], v[0:1], off
	s_movk_i32 s14, 0x13ff
	v_lshlrev_b32_e32 v0, 13, v5
	v_add_u32_e32 v1, 0x200, v4
	v_cmp_lt_i32_e32 vcc, s14, v4
	v_lshlrev_b32_e32 v4, 4, v10
	v_sub_u32_e32 v0, v0, v4
	s_or_b64 s[12:13], vcc, s[12:13]
	v_add_u32_e32 v3, 0x800, v3
	v_add_u32_e32 v158, v2, v0
	v_add_u32_e32 v2, 0x2000, v2
	v_mov_b32_e32 v4, v1

.Lstf_1_787:
	s_or_b64 exec, exec, s[14:15]
	v_mul_i32_i24_e32 v10, 0x200, v5
	v_lshlrev_b32_e32 v6, 2, v10
	v_sub_u32_e32 v6, v3, v6
	v_ashrrev_i32_e32 v7, 31, v6
	v_lshl_add_u64 v[0:1], v[6:7], 2, v[0:1]
	global_load_dwordx4 v[114:117], v[0:1], off
	s_movk_i32 s14, 0x13ff
	v_lshlrev_b32_e32 v0, 13, v5
	v_add_u32_e32 v1, 0x200, v4
	v_cmp_lt_i32_e32 vcc, s14, v4
	v_lshlrev_b32_e32 v4, 4, v10
	v_sub_u32_e32 v0, v0, v4
	s_or_b64 s[12:13], vcc, s[12:13]
	v_add_u32_e32 v3, 0x800, v3
	v_add_u32_e32 v159, v2, v0
	v_add_u32_e32 v2, 0x2000, v2
	v_mov_b32_e32 v4, v1

.Lstf_2_787:
	s_or_b64 exec, exec, s[14:15]
	v_mul_i32_i24_e32 v10, 0x200, v5
	v_lshlrev_b32_e32 v6, 2, v10
	v_sub_u32_e32 v6, v3, v6
	v_ashrrev_i32_e32 v7, 31, v6
	v_lshl_add_u64 v[0:1], v[6:7], 2, v[0:1]
	global_load_dwordx4 v[118:121], v[0:1], off
	s_movk_i32 s14, 0x13ff
	v_lshlrev_b32_e32 v0, 13, v5
	v_add_u32_e32 v1, 0x200, v4
	v_cmp_lt_i32_e32 vcc, s14, v4
	v_lshlrev_b32_e32 v4, 4, v10
	v_sub_u32_e32 v0, v0, v4
	s_or_b64 s[12:13], vcc, s[12:13]
	v_add_u32_e32 v3, 0x800, v3
	v_add_u32_e32 v160, v2, v0
	v_add_u32_e32 v2, 0x2000, v2
	v_mov_b32_e32 v4, v1

.Lstf_3_787:
	s_or_b64 exec, exec, s[14:15]
	v_mul_i32_i24_e32 v10, 0x200, v5
	v_lshlrev_b32_e32 v6, 2, v10
	v_sub_u32_e32 v6, v3, v6
	v_ashrrev_i32_e32 v7, 31, v6
	v_lshl_add_u64 v[0:1], v[6:7], 2, v[0:1]
	global_load_dwordx4 v[122:125], v[0:1], off
	s_movk_i32 s14, 0x13ff
	v_lshlrev_b32_e32 v0, 13, v5
	v_add_u32_e32 v1, 0x200, v4
	v_cmp_lt_i32_e32 vcc, s14, v4
	v_lshlrev_b32_e32 v4, 4, v10
	v_sub_u32_e32 v0, v0, v4
	s_or_b64 s[12:13], vcc, s[12:13]
	v_add_u32_e32 v3, 0x800, v3
	v_add_u32_e32 v161, v2, v0
	v_add_u32_e32 v2, 0x2000, v2
	v_mov_b32_e32 v4, v1

.Lstf_4_787:
	s_or_b64 exec, exec, s[14:15]
	v_mul_i32_i24_e32 v10, 0x200, v5
	v_lshlrev_b32_e32 v6, 2, v10
	v_sub_u32_e32 v6, v3, v6
	v_ashrrev_i32_e32 v7, 31, v6
	v_lshl_add_u64 v[0:1], v[6:7], 2, v[0:1]
	global_load_dwordx4 v[126:129], v[0:1], off
	s_movk_i32 s14, 0x13ff
	v_lshlrev_b32_e32 v0, 13, v5
	v_add_u32_e32 v1, 0x200, v4
	v_cmp_lt_i32_e32 vcc, s14, v4
	v_lshlrev_b32_e32 v4, 4, v10
	v_sub_u32_e32 v0, v0, v4
	s_or_b64 s[12:13], vcc, s[12:13]
	v_add_u32_e32 v3, 0x800, v3
	v_add_u32_e32 v162, v2, v0
	v_add_u32_e32 v2, 0x2000, v2
	v_mov_b32_e32 v4, v1

.Lstf_5_787:
	s_or_b64 exec, exec, s[14:15]
	v_mul_i32_i24_e32 v10, 0x200, v5
	v_lshlrev_b32_e32 v6, 2, v10
	v_sub_u32_e32 v6, v3, v6
	v_ashrrev_i32_e32 v7, 31, v6
	v_lshl_add_u64 v[0:1], v[6:7], 2, v[0:1]
	global_load_dwordx4 v[130:133], v[0:1], off
	s_movk_i32 s14, 0x13ff
	v_lshlrev_b32_e32 v0, 13, v5
	v_add_u32_e32 v1, 0x200, v4
	v_cmp_lt_i32_e32 vcc, s14, v4
	v_lshlrev_b32_e32 v4, 4, v10
	v_sub_u32_e32 v0, v0, v4
	s_or_b64 s[12:13], vcc, s[12:13]
	v_add_u32_e32 v3, 0x800, v3
	v_add_u32_e32 v163, v2, v0
	v_add_u32_e32 v2, 0x2000, v2
	v_mov_b32_e32 v4, v1

.Lstf_6_787:
	s_or_b64 exec, exec, s[14:15]
	v_mul_i32_i24_e32 v10, 0x200, v5
	v_lshlrev_b32_e32 v6, 2, v10
	v_sub_u32_e32 v6, v3, v6
	v_ashrrev_i32_e32 v7, 31, v6
	v_lshl_add_u64 v[0:1], v[6:7], 2, v[0:1]
	global_load_dwordx4 v[134:137], v[0:1], off
	s_movk_i32 s14, 0x13ff
	v_lshlrev_b32_e32 v0, 13, v5
	v_add_u32_e32 v1, 0x200, v4
	v_cmp_lt_i32_e32 vcc, s14, v4
	v_lshlrev_b32_e32 v4, 4, v10
	v_sub_u32_e32 v0, v0, v4
	s_or_b64 s[12:13], vcc, s[12:13]
	v_add_u32_e32 v3, 0x800, v3
	v_add_u32_e32 v164, v2, v0
	v_add_u32_e32 v2, 0x2000, v2
	v_mov_b32_e32 v4, v1

.Lstf_7_787:
	s_or_b64 exec, exec, s[14:15]
	v_mul_i32_i24_e32 v10, 0x200, v5
	v_lshlrev_b32_e32 v6, 2, v10
	v_sub_u32_e32 v6, v3, v6
	v_ashrrev_i32_e32 v7, 31, v6
	v_lshl_add_u64 v[0:1], v[6:7], 2, v[0:1]
	global_load_dwordx4 v[138:141], v[0:1], off
	s_movk_i32 s14, 0x13ff
	v_lshlrev_b32_e32 v0, 13, v5
	v_add_u32_e32 v1, 0x200, v4
	v_cmp_lt_i32_e32 vcc, s14, v4
	v_lshlrev_b32_e32 v4, 4, v10
	v_sub_u32_e32 v0, v0, v4
	s_or_b64 s[12:13], vcc, s[12:13]
	v_add_u32_e32 v3, 0x800, v3
	v_add_u32_e32 v165, v2, v0
	v_add_u32_e32 v2, 0x2000, v2
	v_mov_b32_e32 v4, v1

.Lstf_8_787:
	s_or_b64 exec, exec, s[14:15]
	v_mul_i32_i24_e32 v10, 0x200, v5
	v_lshlrev_b32_e32 v6, 2, v10
	v_sub_u32_e32 v6, v3, v6
	v_ashrrev_i32_e32 v7, 31, v6
	v_lshl_add_u64 v[0:1], v[6:7], 2, v[0:1]
	global_load_dwordx4 v[146:149], v[0:1], off
	s_movk_i32 s14, 0x13ff
	v_lshlrev_b32_e32 v0, 13, v5
	v_add_u32_e32 v1, 0x200, v4
	v_cmp_lt_i32_e32 vcc, s14, v4
	v_lshlrev_b32_e32 v4, 4, v10
	v_sub_u32_e32 v0, v0, v4
	s_or_b64 s[12:13], vcc, s[12:13]
	v_add_u32_e32 v3, 0x800, v3
	v_add_u32_e32 v166, v2, v0
	v_add_u32_e32 v2, 0x2000, v2
	v_mov_b32_e32 v4, v1

.Lstf_9_787:
	s_or_b64 exec, exec, s[14:15]
	v_mul_i32_i24_e32 v10, 0x200, v5
	v_lshlrev_b32_e32 v6, 2, v10
	v_sub_u32_e32 v6, v3, v6
	v_ashrrev_i32_e32 v7, 31, v6
	v_lshl_add_u64 v[0:1], v[6:7], 2, v[0:1]
	global_load_dwordx4 v[150:153], v[0:1], off
	s_movk_i32 s14, 0x13ff
	v_lshlrev_b32_e32 v0, 13, v5
	v_add_u32_e32 v1, 0x200, v4
	v_cmp_lt_i32_e32 vcc, s14, v4
	v_lshlrev_b32_e32 v4, 4, v10
	v_sub_u32_e32 v0, v0, v4
	s_or_b64 s[12:13], vcc, s[12:13]
	v_add_u32_e32 v3, 0x800, v3
	v_add_u32_e32 v167, v2, v0
	v_add_u32_e32 v2, 0x2000, v2
	v_mov_b32_e32 v4, v1

.Lstf_10_787:
	s_or_b64 exec, exec, s[14:15]
	v_mul_i32_i24_e32 v10, 0x200, v5
	v_lshlrev_b32_e32 v6, 2, v10
	v_sub_u32_e32 v6, v3, v6
	v_ashrrev_i32_e32 v7, 31, v6
	v_lshl_add_u64 v[0:1], v[6:7], 2, v[0:1]
	global_load_dwordx4 v[154:157], v[0:1], off
	s_movk_i32 s14, 0x13ff
	v_lshlrev_b32_e32 v0, 13, v5
	v_add_u32_e32 v1, 0x200, v4
	v_cmp_lt_i32_e32 vcc, s14, v4
	v_lshlrev_b32_e32 v4, 4, v10
	v_sub_u32_e32 v0, v0, v4
	s_or_b64 s[12:13], vcc, s[12:13]
	v_add_u32_e32 v3, 0x800, v3
	v_add_u32_e32 v168, v2, v0
	v_add_u32_e32 v2, 0x2000, v2
	v_mov_b32_e32 v4, v1
	s_waitcnt vmcnt(10)
	ds_write_b128 v158, v[110:113]
	s_waitcnt vmcnt(9)
	ds_write_b128 v159, v[114:117]
	s_waitcnt vmcnt(8)
	ds_write_b128 v160, v[118:121]
	s_waitcnt vmcnt(7)
	ds_write_b128 v161, v[122:125]
	s_waitcnt vmcnt(6)
	ds_write_b128 v162, v[126:129]
	s_waitcnt vmcnt(5)
	ds_write_b128 v163, v[130:133]
	s_waitcnt vmcnt(4)
	ds_write_b128 v164, v[134:137]
	s_waitcnt vmcnt(3)
	ds_write_b128 v165, v[138:141]
	s_waitcnt vmcnt(2)
	ds_write_b128 v166, v[146:149]
	s_waitcnt vmcnt(1)
	ds_write_b128 v167, v[150:153]
	s_waitcnt vmcnt(0)
	ds_write_b128 v168, v[154:157]

.LBB0_1119:
	s_cmp_le_i32 s90, s16
	s_cselect_b64 s[8:9], -1, 0
	s_cmp_lt_i32 s16, s91
	s_cselect_b64 s[10:11], -1, 0
	s_and_b64 s[0:1], s[10:11], s[8:9]
	s_andn2_b64 vcc, exec, s[0:1]
	s_cbranch_vccnz .LBB0_1186
	v_readlane_b32 s0, v253, 2
	v_readlane_b32 s1, v253, 3
	v_readlane_b32 s2, v253, 4
	v_readlane_b32 s4, v253, 6
	v_readlane_b32 s5, v253, 7
	v_readlane_b32 s6, v253, 8
	v_readlane_b32 s7, v253, 9
	s_mov_b32 s35, s92
	s_mov_b64 s[0:1], s[6:7]
	s_mov_b32 s75, s88
	s_mov_b32 s34, s85
	s_mov_b64 s[16:17], s[4:5]
	s_mov_b32 s2, s84
	s_waitcnt vmcnt(0) lgkmcnt(0)
	v_mbcnt_lo_u32_b32 v110, -1, 0
	v_mbcnt_hi_u32_b32 v110, -1, v110
	v_readlane_b32 s44, v255, 1
	v_lshl_add_u32 v4, s35, 6, v110
	v_mov_b32_e32 v204, v105
	s_movk_i32 s2, 0x1600
	v_readlane_b32 s45, v255, 2
	v_readlane_b32 s3, v253, 5
	v_cmp_gt_i32_e32 vcc, s2, v4
	v_add_u32_e32 v201, 0x14000, v204
	s_mov_b32 s45, s29
	s_and_saveexec_b64 s[2:3], vcc
	s_movk_i32 s24, 0x11ff
	s_movk_i32 s26, 0x13ff
	s_cbranch_execz .LBB0_1131
	v_cndmask_b32_e64 v0, 0, 1, s[82:83]
	v_add_u32_e32 v0, s44, v0
	s_lshl_b64 s[4:5], s[44:45], 13
	v_mul_lo_u32 v104, v0, 3
	s_mul_hi_u32 s7, s44, 3
	s_mul_i32 s6, s44, 3
	v_lshl_add_u32 v5, v4, 3, v201
	v_lshlrev_b32_e32 v6, 2, v4
	s_mov_b64 s[12:13], 0
.Lsti_0_1124:
	v_cmp_lt_i32_e32 vcc, s24, v4
	s_and_saveexec_b64 s[14:15], vcc
	s_xor_b64 s[14:15], exec, s[14:15]
	s_cbranch_execz .Lsti_0_1126
	v_readlane_b32 s52, v253, 2
	v_and_b32_e32 v0, 0x7ffffe00, v4
	v_readlane_b32 s53, v253, 3
	v_readlane_b32 s55, v253, 5
	s_movk_i32 s18, 0x1200
	v_readlane_b32 s54, v253, 4
	v_mov_b32_e32 v1, s55
	v_mov_b32_e32 v2, s53
	v_cmp_eq_u32_e32 vcc, s18, v0
	v_mov_b32_e32 v0, s54
	v_readlane_b32 s56, v253, 6
	v_cndmask_b32_e32 v1, v1, v2, vcc
	v_mov_b32_e32 v2, s52
	v_cndmask_b32_e32 v0, v0, v2, vcc
	v_readlane_b32 s57, v253, 7
	v_readlane_b32 s58, v253, 8
	v_readlane_b32 s59, v253, 9
	v_lshl_add_u64 v[0:1], v[0:1], 0, s[4:5]
.Lsti_0_1126:
	s_or_saveexec_b64 s[14:15], s[14:15]
	v_ashrrev_i32_e32 v2, 31, v4
	v_lshrrev_b32_e32 v2, 23, v2
	v_add_u32_e32 v2, v4, v2
	v_ashrrev_i32_e32 v7, 9, v2
	s_xor_b64 exec, exec, s[14:15]
	s_cbranch_execz .Lsti_0_1123
	s_mov_b32 s18, 0x2aaaaaab
	v_mul_hi_i32 v0, v4, s18
	v_lshrrev_b32_e32 v1, 31, v0
	v_ashrrev_i32_e32 v0, 8, v0
	s_mov_b32 s18, 0x55555556
	v_add_u32_e32 v2, v0, v1
	v_mul_hi_i32 v0, v7, s18
	v_lshrrev_b32_e32 v1, 31, v0
	v_add_u32_e32 v0, v0, v1
	v_lshl_add_u32 v0, v0, 1, v0
	v_sub_u32_e32 v8, v7, v0
	v_cmp_ne_u32_e32 vcc, 0, v8
	v_ashrrev_i32_e32 v3, 31, v2
	s_and_saveexec_b64 s[18:19], vcc
	s_xor_b64 s[18:19], exec, s[18:19]
	v_lshl_add_u64 v[0:1], v[2:3], 0, v[104:105]
	v_mov_b64_e32 v[2:3], s[0:1]
	v_mad_u64_u32 v[2:3], s[40:41], v0, s93, v[2:3]
	v_lshlrev_b32_e32 v0, 11, v8
	v_mad_i32_i24 v3, v1, s93, v3
	v_ashrrev_i32_e32 v1, 31, v0
	v_lshl_add_u64 v[0:1], v[0:1], 2, v[2:3]
	s_mov_b64 s[40:41], 0xfe000
	v_lshl_add_u64 v[0:1], v[0:1], 0, s[40:41]
	s_andn2_saveexec_b64 s[18:19], s[18:19]
	s_cbranch_execz .Lsti_0_1122
	v_lshl_add_u64 v[0:1], s[6:7], 0, v[2:3]
	v_mov_b64_e32 v[2:3], s[0:1]
	v_mad_u64_u32 v[2:3], s[40:41], v0, s93, v[2:3]
	v_mad_i32_i24 v3, v1, s93, v3
	s_mov_b64 s[40:41], 0x10a000
	v_lshl_add_u64 v[0:1], v[2:3], 0, s[40:41]
	s_branch .Lsti_0_1122
.Lsti_0_1122:
	s_or_b64 exec, exec, s[18:19]
.Lsti_0_1123:
	s_or_b64 exec, exec, s[14:15]
	v_mul_i32_i24_e32 v8, 0x200, v7
	v_lshlrev_b32_e32 v2, 2, v8
	v_sub_u32_e32 v2, v6, v2
	v_ashrrev_i32_e32 v3, 31, v2
	v_lshl_add_u64 v[0:1], v[2:3], 2, v[0:1]
	global_load_dwordx4 v[12:15], v[0:1], off
	v_lshlrev_b32_e32 v7, 12, v7
	v_add_u32_e32 v9, 0x200, v4
	v_cmp_lt_i32_e32 vcc, s26, v4
	v_lshlrev_b32_e32 v4, 3, v8
	v_sub_u32_e32 v4, v7, v4
	v_add_u32_e32 v56, v5, v4
	s_or_b64 s[12:13], vcc, s[12:13]
	v_add_u32_e32 v6, 0x800, v6
	v_add_u32_e32 v5, 0x1000, v5
	v_mov_b32_e32 v4, v9

.Lsti_1_1126:
	s_or_saveexec_b64 s[14:15], s[14:15]
	v_ashrrev_i32_e32 v2, 31, v4
	v_lshrrev_b32_e32 v2, 23, v2
	v_add_u32_e32 v2, v4, v2
	v_ashrrev_i32_e32 v7, 9, v2
	s_xor_b64 exec, exec, s[14:15]
	s_cbranch_execz .Lsti_1_1123
	s_mov_b32 s18, 0x2aaaaaab
	v_mul_hi_i32 v0, v4, s18
	v_lshrrev_b32_e32 v1, 31, v0
	v_ashrrev_i32_e32 v0, 8, v0
	s_mov_b32 s18, 0x55555556
	v_add_u32_e32 v2, v0, v1
	v_mul_hi_i32 v0, v7, s18
	v_lshrrev_b32_e32 v1, 31, v0
	v_add_u32_e32 v0, v0, v1
	v_lshl_add_u32 v0, v0, 1, v0
	v_sub_u32_e32 v8, v7, v0
	v_cmp_ne_u32_e32 vcc, 0, v8
	v_ashrrev_i32_e32 v3, 31, v2
	s_and_saveexec_b64 s[18:19], vcc
	s_xor_b64 s[18:19], exec, s[18:19]
	v_lshl_add_u64 v[0:1], v[2:3], 0, v[104:105]
	v_mov_b64_e32 v[2:3], s[0:1]
	v_mad_u64_u32 v[2:3], s[40:41], v0, s93, v[2:3]
	v_lshlrev_b32_e32 v0, 11, v8
	v_mad_i32_i24 v3, v1, s93, v3
	v_ashrrev_i32_e32 v1, 31, v0
	v_lshl_add_u64 v[0:1], v[0:1], 2, v[2:3]
	s_mov_b64 s[40:41], 0xfe000
	v_lshl_add_u64 v[0:1], v[0:1], 0, s[40:41]
	s_andn2_saveexec_b64 s[18:19], s[18:19]
	s_cbranch_execz .Lsti_1_1122
	v_lshl_add_u64 v[0:1], s[6:7], 0, v[2:3]
	v_mov_b64_e32 v[2:3], s[0:1]
	v_mad_u64_u32 v[2:3], s[40:41], v0, s93, v[2:3]
	v_mad_i32_i24 v3, v1, s93, v3
	s_mov_b64 s[40:41], 0x10a000
	v_lshl_add_u64 v[0:1], v[2:3], 0, s[40:41]
	s_branch .Lsti_1_1122
.Lsti_1_1122:
	s_or_b64 exec, exec, s[18:19]
.Lsti_1_1123:
	s_or_b64 exec, exec, s[14:15]
	v_mul_i32_i24_e32 v8, 0x200, v7
	v_lshlrev_b32_e32 v2, 2, v8
	v_sub_u32_e32 v2, v6, v2
	v_ashrrev_i32_e32 v3, 31, v2
	v_lshl_add_u64 v[0:1], v[2:3], 2, v[0:1]
	global_load_dwordx4 v[16:19], v[0:1], off
	v_lshlrev_b32_e32 v7, 12, v7
	v_add_u32_e32 v9, 0x200, v4
	v_cmp_lt_i32_e32 vcc, s26, v4
	v_lshlrev_b32_e32 v4, 3, v8
	v_sub_u32_e32 v4, v7, v4
	v_add_u32_e32 v57, v5, v4
	s_or_b64 s[12:13], vcc, s[12:13]
	v_add_u32_e32 v6, 0x800, v6
	v_add_u32_e32 v5, 0x1000, v5
	v_mov_b32_e32 v4, v9

.Lsti_2_1126:
	s_or_saveexec_b64 s[14:15], s[14:15]
	v_ashrrev_i32_e32 v2, 31, v4
	v_lshrrev_b32_e32 v2, 23, v2
	v_add_u32_e32 v2, v4, v2
	v_ashrrev_i32_e32 v7, 9, v2
	s_xor_b64 exec, exec, s[14:15]
	s_cbranch_execz .Lsti_2_1123
	s_mov_b32 s18, 0x2aaaaaab
	v_mul_hi_i32 v0, v4, s18
	v_lshrrev_b32_e32 v1, 31, v0
	v_ashrrev_i32_e32 v0, 8, v0
	s_mov_b32 s18, 0x55555556
	v_add_u32_e32 v2, v0, v1
	v_mul_hi_i32 v0, v7, s18
	v_lshrrev_b32_e32 v1, 31, v0
	v_add_u32_e32 v0, v0, v1
	v_lshl_add_u32 v0, v0, 1, v0
	v_sub_u32_e32 v8, v7, v0
	v_cmp_ne_u32_e32 vcc, 0, v8
	v_ashrrev_i32_e32 v3, 31, v2
	s_and_saveexec_b64 s[18:19], vcc
	s_xor_b64 s[18:19], exec, s[18:19]
	v_lshl_add_u64 v[0:1], v[2:3], 0, v[104:105]
	v_mov_b64_e32 v[2:3], s[0:1]
	v_mad_u64_u32 v[2:3], s[40:41], v0, s93, v[2:3]
	v_lshlrev_b32_e32 v0, 11, v8
	v_mad_i32_i24 v3, v1, s93, v3
	v_ashrrev_i32_e32 v1, 31, v0
	v_lshl_add_u64 v[0:1], v[0:1], 2, v[2:3]
	s_mov_b64 s[40:41], 0xfe000
	v_lshl_add_u64 v[0:1], v[0:1], 0, s[40:41]
	s_andn2_saveexec_b64 s[18:19], s[18:19]
	s_cbranch_execz .Lsti_2_1122
	v_lshl_add_u64 v[0:1], s[6:7], 0, v[2:3]
	v_mov_b64_e32 v[2:3], s[0:1]
	v_mad_u64_u32 v[2:3], s[40:41], v0, s93, v[2:3]
	v_mad_i32_i24 v3, v1, s93, v3
	s_mov_b64 s[40:41], 0x10a000
	v_lshl_add_u64 v[0:1], v[2:3], 0, s[40:41]
	s_branch .Lsti_2_1122
.Lsti_2_1122:
	s_or_b64 exec, exec, s[18:19]
.Lsti_2_1123:
	s_or_b64 exec, exec, s[14:15]
	v_mul_i32_i24_e32 v8, 0x200, v7
	v_lshlrev_b32_e32 v2, 2, v8
	v_sub_u32_e32 v2, v6, v2
	v_ashrrev_i32_e32 v3, 31, v2
	v_lshl_add_u64 v[0:1], v[2:3], 2, v[0:1]
	global_load_dwordx4 v[20:23], v[0:1], off
	v_lshlrev_b32_e32 v7, 12, v7
	v_add_u32_e32 v9, 0x200, v4
	v_cmp_lt_i32_e32 vcc, s26, v4
	v_lshlrev_b32_e32 v4, 3, v8
	v_sub_u32_e32 v4, v7, v4
	v_add_u32_e32 v58, v5, v4
	s_or_b64 s[12:13], vcc, s[12:13]
	v_add_u32_e32 v6, 0x800, v6
	v_add_u32_e32 v5, 0x1000, v5
	v_mov_b32_e32 v4, v9

.Lsti_3_1126:
	s_or_saveexec_b64 s[14:15], s[14:15]
	v_ashrrev_i32_e32 v2, 31, v4
	v_lshrrev_b32_e32 v2, 23, v2
	v_add_u32_e32 v2, v4, v2
	v_ashrrev_i32_e32 v7, 9, v2
	s_xor_b64 exec, exec, s[14:15]
	s_cbranch_execz .Lsti_3_1123
	s_mov_b32 s18, 0x2aaaaaab
	v_mul_hi_i32 v0, v4, s18
	v_lshrrev_b32_e32 v1, 31, v0
	v_ashrrev_i32_e32 v0, 8, v0
	s_mov_b32 s18, 0x55555556
	v_add_u32_e32 v2, v0, v1
	v_mul_hi_i32 v0, v7, s18
	v_lshrrev_b32_e32 v1, 31, v0
	v_add_u32_e32 v0, v0, v1
	v_lshl_add_u32 v0, v0, 1, v0
	v_sub_u32_e32 v8, v7, v0
	v_cmp_ne_u32_e32 vcc, 0, v8
	v_ashrrev_i32_e32 v3, 31, v2
	s_and_saveexec_b64 s[18:19], vcc
	s_xor_b64 s[18:19], exec, s[18:19]
	v_lshl_add_u64 v[0:1], v[2:3], 0, v[104:105]
	v_mov_b64_e32 v[2:3], s[0:1]
	v_mad_u64_u32 v[2:3], s[40:41], v0, s93, v[2:3]
	v_lshlrev_b32_e32 v0, 11, v8
	v_mad_i32_i24 v3, v1, s93, v3
	v_ashrrev_i32_e32 v1, 31, v0
	v_lshl_add_u64 v[0:1], v[0:1], 2, v[2:3]
	s_mov_b64 s[40:41], 0xfe000
	v_lshl_add_u64 v[0:1], v[0:1], 0, s[40:41]
	s_andn2_saveexec_b64 s[18:19], s[18:19]
	s_cbranch_execz .Lsti_3_1122
	v_lshl_add_u64 v[0:1], s[6:7], 0, v[2:3]
	v_mov_b64_e32 v[2:3], s[0:1]
	v_mad_u64_u32 v[2:3], s[40:41], v0, s93, v[2:3]
	v_mad_i32_i24 v3, v1, s93, v3
	s_mov_b64 s[40:41], 0x10a000
	v_lshl_add_u64 v[0:1], v[2:3], 0, s[40:41]
	s_branch .Lsti_3_1122
.Lsti_3_1122:
	s_or_b64 exec, exec, s[18:19]
.Lsti_3_1123:
	s_or_b64 exec, exec, s[14:15]
	v_mul_i32_i24_e32 v8, 0x200, v7
	v_lshlrev_b32_e32 v2, 2, v8
	v_sub_u32_e32 v2, v6, v2
	v_ashrrev_i32_e32 v3, 31, v2
	v_lshl_add_u64 v[0:1], v[2:3], 2, v[0:1]
	global_load_dwordx4 v[24:27], v[0:1], off
	v_lshlrev_b32_e32 v7, 12, v7
	v_add_u32_e32 v9, 0x200, v4
	v_cmp_lt_i32_e32 vcc, s26, v4
	v_lshlrev_b32_e32 v4, 3, v8
	v_sub_u32_e32 v4, v7, v4
	v_add_u32_e32 v59, v5, v4
	s_or_b64 s[12:13], vcc, s[12:13]
	v_add_u32_e32 v6, 0x800, v6
	v_add_u32_e32 v5, 0x1000, v5
	v_mov_b32_e32 v4, v9

.Lsti_4_1126:
	s_or_saveexec_b64 s[14:15], s[14:15]
	v_ashrrev_i32_e32 v2, 31, v4
	v_lshrrev_b32_e32 v2, 23, v2
	v_add_u32_e32 v2, v4, v2
	v_ashrrev_i32_e32 v7, 9, v2
	s_xor_b64 exec, exec, s[14:15]
	s_cbranch_execz .Lsti_4_1123
	s_mov_b32 s18, 0x2aaaaaab
	v_mul_hi_i32 v0, v4, s18
	v_lshrrev_b32_e32 v1, 31, v0
	v_ashrrev_i32_e32 v0, 8, v0
	s_mov_b32 s18, 0x55555556
	v_add_u32_e32 v2, v0, v1
	v_mul_hi_i32 v0, v7, s18
	v_lshrrev_b32_e32 v1, 31, v0
	v_add_u32_e32 v0, v0, v1
	v_lshl_add_u32 v0, v0, 1, v0
	v_sub_u32_e32 v8, v7, v0
	v_cmp_ne_u32_e32 vcc, 0, v8
	v_ashrrev_i32_e32 v3, 31, v2
	s_and_saveexec_b64 s[18:19], vcc
	s_xor_b64 s[18:19], exec, s[18:19]
	v_lshl_add_u64 v[0:1], v[2:3], 0, v[104:105]
	v_mov_b64_e32 v[2:3], s[0:1]
	v_mad_u64_u32 v[2:3], s[40:41], v0, s93, v[2:3]
	v_lshlrev_b32_e32 v0, 11, v8
	v_mad_i32_i24 v3, v1, s93, v3
	v_ashrrev_i32_e32 v1, 31, v0
	v_lshl_add_u64 v[0:1], v[0:1], 2, v[2:3]
	s_mov_b64 s[40:41], 0xfe000
	v_lshl_add_u64 v[0:1], v[0:1], 0, s[40:41]
	s_andn2_saveexec_b64 s[18:19], s[18:19]
	s_cbranch_execz .Lsti_4_1122
	v_lshl_add_u64 v[0:1], s[6:7], 0, v[2:3]
	v_mov_b64_e32 v[2:3], s[0:1]
	v_mad_u64_u32 v[2:3], s[40:41], v0, s93, v[2:3]
	v_mad_i32_i24 v3, v1, s93, v3
	s_mov_b64 s[40:41], 0x10a000
	v_lshl_add_u64 v[0:1], v[2:3], 0, s[40:41]
	s_branch .Lsti_4_1122
.Lsti_4_1122:
	s_or_b64 exec, exec, s[18:19]
.Lsti_4_1123:
	s_or_b64 exec, exec, s[14:15]
	v_mul_i32_i24_e32 v8, 0x200, v7
	v_lshlrev_b32_e32 v2, 2, v8
	v_sub_u32_e32 v2, v6, v2
	v_ashrrev_i32_e32 v3, 31, v2
	v_lshl_add_u64 v[0:1], v[2:3], 2, v[0:1]
	global_load_dwordx4 v[28:31], v[0:1], off
	v_lshlrev_b32_e32 v7, 12, v7
	v_add_u32_e32 v9, 0x200, v4
	v_cmp_lt_i32_e32 vcc, s26, v4
	v_lshlrev_b32_e32 v4, 3, v8
	v_sub_u32_e32 v4, v7, v4
	v_add_u32_e32 v60, v5, v4
	s_or_b64 s[12:13], vcc, s[12:13]
	v_add_u32_e32 v6, 0x800, v6
	v_add_u32_e32 v5, 0x1000, v5
	v_mov_b32_e32 v4, v9

.Lsti_5_1126:
	s_or_saveexec_b64 s[14:15], s[14:15]
	v_ashrrev_i32_e32 v2, 31, v4
	v_lshrrev_b32_e32 v2, 23, v2
	v_add_u32_e32 v2, v4, v2
	v_ashrrev_i32_e32 v7, 9, v2
	s_xor_b64 exec, exec, s[14:15]
	s_cbranch_execz .Lsti_5_1123
	s_mov_b32 s18, 0x2aaaaaab
	v_mul_hi_i32 v0, v4, s18
	v_lshrrev_b32_e32 v1, 31, v0
	v_ashrrev_i32_e32 v0, 8, v0
	s_mov_b32 s18, 0x55555556
	v_add_u32_e32 v2, v0, v1
	v_mul_hi_i32 v0, v7, s18
	v_lshrrev_b32_e32 v1, 31, v0
	v_add_u32_e32 v0, v0, v1
	v_lshl_add_u32 v0, v0, 1, v0
	v_sub_u32_e32 v8, v7, v0
	v_cmp_ne_u32_e32 vcc, 0, v8
	v_ashrrev_i32_e32 v3, 31, v2
	s_and_saveexec_b64 s[18:19], vcc
	s_xor_b64 s[18:19], exec, s[18:19]
	v_lshl_add_u64 v[0:1], v[2:3], 0, v[104:105]
	v_mov_b64_e32 v[2:3], s[0:1]
	v_mad_u64_u32 v[2:3], s[40:41], v0, s93, v[2:3]
	v_lshlrev_b32_e32 v0, 11, v8
	v_mad_i32_i24 v3, v1, s93, v3
	v_ashrrev_i32_e32 v1, 31, v0
	v_lshl_add_u64 v[0:1], v[0:1], 2, v[2:3]
	s_mov_b64 s[40:41], 0xfe000
	v_lshl_add_u64 v[0:1], v[0:1], 0, s[40:41]
	s_andn2_saveexec_b64 s[18:19], s[18:19]
	s_cbranch_execz .Lsti_5_1122
	v_lshl_add_u64 v[0:1], s[6:7], 0, v[2:3]
	v_mov_b64_e32 v[2:3], s[0:1]
	v_mad_u64_u32 v[2:3], s[40:41], v0, s93, v[2:3]
	v_mad_i32_i24 v3, v1, s93, v3
	s_mov_b64 s[40:41], 0x10a000
	v_lshl_add_u64 v[0:1], v[2:3], 0, s[40:41]
	s_branch .Lsti_5_1122
.Lsti_5_1122:
	s_or_b64 exec, exec, s[18:19]
.Lsti_5_1123:
	s_or_b64 exec, exec, s[14:15]
	v_mul_i32_i24_e32 v8, 0x200, v7
	v_lshlrev_b32_e32 v2, 2, v8
	v_sub_u32_e32 v2, v6, v2
	v_ashrrev_i32_e32 v3, 31, v2
	v_lshl_add_u64 v[0:1], v[2:3], 2, v[0:1]
	global_load_dwordx4 v[32:35], v[0:1], off
	v_lshlrev_b32_e32 v7, 12, v7
	v_add_u32_e32 v9, 0x200, v4
	v_cmp_lt_i32_e32 vcc, s26, v4
	v_lshlrev_b32_e32 v4, 3, v8
	v_sub_u32_e32 v4, v7, v4
	v_add_u32_e32 v61, v5, v4
	s_or_b64 s[12:13], vcc, s[12:13]
	v_add_u32_e32 v6, 0x800, v6
	v_add_u32_e32 v5, 0x1000, v5
	v_mov_b32_e32 v4, v9

.Lsti_6_1126:
	s_or_saveexec_b64 s[14:15], s[14:15]
	v_ashrrev_i32_e32 v2, 31, v4
	v_lshrrev_b32_e32 v2, 23, v2
	v_add_u32_e32 v2, v4, v2
	v_ashrrev_i32_e32 v7, 9, v2
	s_xor_b64 exec, exec, s[14:15]
	s_cbranch_execz .Lsti_6_1123
	s_mov_b32 s18, 0x2aaaaaab
	v_mul_hi_i32 v0, v4, s18
	v_lshrrev_b32_e32 v1, 31, v0
	v_ashrrev_i32_e32 v0, 8, v0
	s_mov_b32 s18, 0x55555556
	v_add_u32_e32 v2, v0, v1
	v_mul_hi_i32 v0, v7, s18
	v_lshrrev_b32_e32 v1, 31, v0
	v_add_u32_e32 v0, v0, v1
	v_lshl_add_u32 v0, v0, 1, v0
	v_sub_u32_e32 v8, v7, v0
	v_cmp_ne_u32_e32 vcc, 0, v8
	v_ashrrev_i32_e32 v3, 31, v2
	s_and_saveexec_b64 s[18:19], vcc
	s_xor_b64 s[18:19], exec, s[18:19]
	v_lshl_add_u64 v[0:1], v[2:3], 0, v[104:105]
	v_mov_b64_e32 v[2:3], s[0:1]
	v_mad_u64_u32 v[2:3], s[40:41], v0, s93, v[2:3]
	v_lshlrev_b32_e32 v0, 11, v8
	v_mad_i32_i24 v3, v1, s93, v3
	v_ashrrev_i32_e32 v1, 31, v0
	v_lshl_add_u64 v[0:1], v[0:1], 2, v[2:3]
	s_mov_b64 s[40:41], 0xfe000
	v_lshl_add_u64 v[0:1], v[0:1], 0, s[40:41]
	s_andn2_saveexec_b64 s[18:19], s[18:19]
	s_cbranch_execz .Lsti_6_1122
	v_lshl_add_u64 v[0:1], s[6:7], 0, v[2:3]
	v_mov_b64_e32 v[2:3], s[0:1]
	v_mad_u64_u32 v[2:3], s[40:41], v0, s93, v[2:3]
	v_mad_i32_i24 v3, v1, s93, v3
	s_mov_b64 s[40:41], 0x10a000
	v_lshl_add_u64 v[0:1], v[2:3], 0, s[40:41]
	s_branch .Lsti_6_1122
.Lsti_6_1122:
	s_or_b64 exec, exec, s[18:19]
.Lsti_6_1123:
	s_or_b64 exec, exec, s[14:15]
	v_mul_i32_i24_e32 v8, 0x200, v7
	v_lshlrev_b32_e32 v2, 2, v8
	v_sub_u32_e32 v2, v6, v2
	v_ashrrev_i32_e32 v3, 31, v2
	v_lshl_add_u64 v[0:1], v[2:3], 2, v[0:1]
	global_load_dwordx4 v[36:39], v[0:1], off
	v_lshlrev_b32_e32 v7, 12, v7
	v_add_u32_e32 v9, 0x200, v4
	v_cmp_lt_i32_e32 vcc, s26, v4
	v_lshlrev_b32_e32 v4, 3, v8
	v_sub_u32_e32 v4, v7, v4
	v_add_u32_e32 v62, v5, v4
	s_or_b64 s[12:13], vcc, s[12:13]
	v_add_u32_e32 v6, 0x800, v6
	v_add_u32_e32 v5, 0x1000, v5
	v_mov_b32_e32 v4, v9

.Lsti_7_1126:
	s_or_saveexec_b64 s[14:15], s[14:15]
	v_ashrrev_i32_e32 v2, 31, v4
	v_lshrrev_b32_e32 v2, 23, v2
	v_add_u32_e32 v2, v4, v2
	v_ashrrev_i32_e32 v7, 9, v2
	s_xor_b64 exec, exec, s[14:15]
	s_cbranch_execz .Lsti_7_1123
	s_mov_b32 s18, 0x2aaaaaab
	v_mul_hi_i32 v0, v4, s18
	v_lshrrev_b32_e32 v1, 31, v0
	v_ashrrev_i32_e32 v0, 8, v0
	s_mov_b32 s18, 0x55555556
	v_add_u32_e32 v2, v0, v1
	v_mul_hi_i32 v0, v7, s18
	v_lshrrev_b32_e32 v1, 31, v0
	v_add_u32_e32 v0, v0, v1
	v_lshl_add_u32 v0, v0, 1, v0
	v_sub_u32_e32 v8, v7, v0
	v_cmp_ne_u32_e32 vcc, 0, v8
	v_ashrrev_i32_e32 v3, 31, v2
	s_and_saveexec_b64 s[18:19], vcc
	s_xor_b64 s[18:19], exec, s[18:19]
	v_lshl_add_u64 v[0:1], v[2:3], 0, v[104:105]
	v_mov_b64_e32 v[2:3], s[0:1]
	v_mad_u64_u32 v[2:3], s[40:41], v0, s93, v[2:3]
	v_lshlrev_b32_e32 v0, 11, v8
	v_mad_i32_i24 v3, v1, s93, v3
	v_ashrrev_i32_e32 v1, 31, v0
	v_lshl_add_u64 v[0:1], v[0:1], 2, v[2:3]
	s_mov_b64 s[40:41], 0xfe000
	v_lshl_add_u64 v[0:1], v[0:1], 0, s[40:41]
	s_andn2_saveexec_b64 s[18:19], s[18:19]
	s_cbranch_execz .Lsti_7_1122
	v_lshl_add_u64 v[0:1], s[6:7], 0, v[2:3]
	v_mov_b64_e32 v[2:3], s[0:1]
	v_mad_u64_u32 v[2:3], s[40:41], v0, s93, v[2:3]
	v_mad_i32_i24 v3, v1, s93, v3
	s_mov_b64 s[40:41], 0x10a000
	v_lshl_add_u64 v[0:1], v[2:3], 0, s[40:41]
	s_branch .Lsti_7_1122
.Lsti_7_1122:
	s_or_b64 exec, exec, s[18:19]
.Lsti_7_1123:
	s_or_b64 exec, exec, s[14:15]
	v_mul_i32_i24_e32 v8, 0x200, v7
	v_lshlrev_b32_e32 v2, 2, v8
	v_sub_u32_e32 v2, v6, v2
	v_ashrrev_i32_e32 v3, 31, v2
	v_lshl_add_u64 v[0:1], v[2:3], 2, v[0:1]
	global_load_dwordx4 v[40:43], v[0:1], off
	v_lshlrev_b32_e32 v7, 12, v7
	v_add_u32_e32 v9, 0x200, v4
	v_cmp_lt_i32_e32 vcc, s26, v4
	v_lshlrev_b32_e32 v4, 3, v8
	v_sub_u32_e32 v4, v7, v4
	v_add_u32_e32 v63, v5, v4
	s_or_b64 s[12:13], vcc, s[12:13]
	v_add_u32_e32 v6, 0x800, v6
	v_add_u32_e32 v5, 0x1000, v5
	v_mov_b32_e32 v4, v9

.Lsti_8_1126:
	s_or_saveexec_b64 s[14:15], s[14:15]
	v_ashrrev_i32_e32 v2, 31, v4
	v_lshrrev_b32_e32 v2, 23, v2
	v_add_u32_e32 v2, v4, v2
	v_ashrrev_i32_e32 v7, 9, v2
	s_xor_b64 exec, exec, s[14:15]
	s_cbranch_execz .Lsti_8_1123
	s_mov_b32 s18, 0x2aaaaaab
	v_mul_hi_i32 v0, v4, s18
	v_lshrrev_b32_e32 v1, 31, v0
	v_ashrrev_i32_e32 v0, 8, v0
	s_mov_b32 s18, 0x55555556
	v_add_u32_e32 v2, v0, v1
	v_mul_hi_i32 v0, v7, s18
	v_lshrrev_b32_e32 v1, 31, v0
	v_add_u32_e32 v0, v0, v1
	v_lshl_add_u32 v0, v0, 1, v0
	v_sub_u32_e32 v8, v7, v0
	v_cmp_ne_u32_e32 vcc, 0, v8
	v_ashrrev_i32_e32 v3, 31, v2
	s_and_saveexec_b64 s[18:19], vcc
	s_xor_b64 s[18:19], exec, s[18:19]
	v_lshl_add_u64 v[0:1], v[2:3], 0, v[104:105]
	v_mov_b64_e32 v[2:3], s[0:1]
	v_mad_u64_u32 v[2:3], s[40:41], v0, s93, v[2:3]
	v_lshlrev_b32_e32 v0, 11, v8
	v_mad_i32_i24 v3, v1, s93, v3
	v_ashrrev_i32_e32 v1, 31, v0
	v_lshl_add_u64 v[0:1], v[0:1], 2, v[2:3]
	s_mov_b64 s[40:41], 0xfe000
	v_lshl_add_u64 v[0:1], v[0:1], 0, s[40:41]
	s_andn2_saveexec_b64 s[18:19], s[18:19]
	s_cbranch_execz .Lsti_8_1122
	v_lshl_add_u64 v[0:1], s[6:7], 0, v[2:3]
	v_mov_b64_e32 v[2:3], s[0:1]
	v_mad_u64_u32 v[2:3], s[40:41], v0, s93, v[2:3]
	v_mad_i32_i24 v3, v1, s93, v3
	s_mov_b64 s[40:41], 0x10a000
	v_lshl_add_u64 v[0:1], v[2:3], 0, s[40:41]
	s_branch .Lsti_8_1122
.Lsti_8_1122:
	s_or_b64 exec, exec, s[18:19]
.Lsti_8_1123:
	s_or_b64 exec, exec, s[14:15]
	v_mul_i32_i24_e32 v8, 0x200, v7
	v_lshlrev_b32_e32 v2, 2, v8
	v_sub_u32_e32 v2, v6, v2
	v_ashrrev_i32_e32 v3, 31, v2
	v_lshl_add_u64 v[0:1], v[2:3], 2, v[0:1]
	global_load_dwordx4 v[44:47], v[0:1], off
	v_lshlrev_b32_e32 v7, 12, v7
	v_add_u32_e32 v9, 0x200, v4
	v_cmp_lt_i32_e32 vcc, s26, v4
	v_lshlrev_b32_e32 v4, 3, v8
	v_sub_u32_e32 v4, v7, v4
	v_add_u32_e32 v64, v5, v4
	s_or_b64 s[12:13], vcc, s[12:13]
	v_add_u32_e32 v6, 0x800, v6
	v_add_u32_e32 v5, 0x1000, v5
	v_mov_b32_e32 v4, v9

.Lsti_9_1126:
	s_or_saveexec_b64 s[14:15], s[14:15]
	v_ashrrev_i32_e32 v2, 31, v4
	v_lshrrev_b32_e32 v2, 23, v2
	v_add_u32_e32 v2, v4, v2
	v_ashrrev_i32_e32 v7, 9, v2
	s_xor_b64 exec, exec, s[14:15]
	s_cbranch_execz .Lsti_9_1123
	s_mov_b32 s18, 0x2aaaaaab
	v_mul_hi_i32 v0, v4, s18
	v_lshrrev_b32_e32 v1, 31, v0
	v_ashrrev_i32_e32 v0, 8, v0
	s_mov_b32 s18, 0x55555556
	v_add_u32_e32 v2, v0, v1
	v_mul_hi_i32 v0, v7, s18
	v_lshrrev_b32_e32 v1, 31, v0
	v_add_u32_e32 v0, v0, v1
	v_lshl_add_u32 v0, v0, 1, v0
	v_sub_u32_e32 v8, v7, v0
	v_cmp_ne_u32_e32 vcc, 0, v8
	v_ashrrev_i32_e32 v3, 31, v2
	s_and_saveexec_b64 s[18:19], vcc
	s_xor_b64 s[18:19], exec, s[18:19]
	v_lshl_add_u64 v[0:1], v[2:3], 0, v[104:105]
	v_mov_b64_e32 v[2:3], s[0:1]
	v_mad_u64_u32 v[2:3], s[40:41], v0, s93, v[2:3]
	v_lshlrev_b32_e32 v0, 11, v8
	v_mad_i32_i24 v3, v1, s93, v3
	v_ashrrev_i32_e32 v1, 31, v0
	v_lshl_add_u64 v[0:1], v[0:1], 2, v[2:3]
	s_mov_b64 s[40:41], 0xfe000
	v_lshl_add_u64 v[0:1], v[0:1], 0, s[40:41]
	s_andn2_saveexec_b64 s[18:19], s[18:19]
	s_cbranch_execz .Lsti_9_1122
	v_lshl_add_u64 v[0:1], s[6:7], 0, v[2:3]
	v_mov_b64_e32 v[2:3], s[0:1]
	v_mad_u64_u32 v[2:3], s[40:41], v0, s93, v[2:3]
	v_mad_i32_i24 v3, v1, s93, v3
	s_mov_b64 s[40:41], 0x10a000
	v_lshl_add_u64 v[0:1], v[2:3], 0, s[40:41]
	s_branch .Lsti_9_1122
.Lsti_9_1122:
	s_or_b64 exec, exec, s[18:19]
.Lsti_9_1123:
	s_or_b64 exec, exec, s[14:15]
	v_mul_i32_i24_e32 v8, 0x200, v7
	v_lshlrev_b32_e32 v2, 2, v8
	v_sub_u32_e32 v2, v6, v2
	v_ashrrev_i32_e32 v3, 31, v2
	v_lshl_add_u64 v[0:1], v[2:3], 2, v[0:1]
	global_load_dwordx4 v[48:51], v[0:1], off
	v_lshlrev_b32_e32 v7, 12, v7
	v_add_u32_e32 v9, 0x200, v4
	v_cmp_lt_i32_e32 vcc, s26, v4
	v_lshlrev_b32_e32 v4, 3, v8
	v_sub_u32_e32 v4, v7, v4
	v_add_u32_e32 v65, v5, v4
	s_or_b64 s[12:13], vcc, s[12:13]
	v_add_u32_e32 v6, 0x800, v6
	v_add_u32_e32 v5, 0x1000, v5
	v_mov_b32_e32 v4, v9

.Lsti_10_1126:
	s_or_saveexec_b64 s[14:15], s[14:15]
	v_ashrrev_i32_e32 v2, 31, v4
	v_lshrrev_b32_e32 v2, 23, v2
	v_add_u32_e32 v2, v4, v2
	v_ashrrev_i32_e32 v7, 9, v2
	s_xor_b64 exec, exec, s[14:15]
	s_cbranch_execz .Lsti_10_1123
	s_mov_b32 s18, 0x2aaaaaab
	v_mul_hi_i32 v0, v4, s18
	v_lshrrev_b32_e32 v1, 31, v0
	v_ashrrev_i32_e32 v0, 8, v0
	s_mov_b32 s18, 0x55555556
	v_add_u32_e32 v2, v0, v1
	v_mul_hi_i32 v0, v7, s18
	v_lshrrev_b32_e32 v1, 31, v0
	v_add_u32_e32 v0, v0, v1
	v_lshl_add_u32 v0, v0, 1, v0
	v_sub_u32_e32 v8, v7, v0
	v_cmp_ne_u32_e32 vcc, 0, v8
	v_ashrrev_i32_e32 v3, 31, v2
	s_and_saveexec_b64 s[18:19], vcc
	s_xor_b64 s[18:19], exec, s[18:19]
	v_lshl_add_u64 v[0:1], v[2:3], 0, v[104:105]
	v_mov_b64_e32 v[2:3], s[0:1]
	v_mad_u64_u32 v[2:3], s[40:41], v0, s93, v[2:3]
	v_lshlrev_b32_e32 v0, 11, v8
	v_mad_i32_i24 v3, v1, s93, v3
	v_ashrrev_i32_e32 v1, 31, v0
	v_lshl_add_u64 v[0:1], v[0:1], 2, v[2:3]
	s_mov_b64 s[40:41], 0xfe000
	v_lshl_add_u64 v[0:1], v[0:1], 0, s[40:41]
	s_andn2_saveexec_b64 s[18:19], s[18:19]
	s_cbranch_execz .Lsti_10_1122
	v_lshl_add_u64 v[0:1], s[6:7], 0, v[2:3]
	v_mov_b64_e32 v[2:3], s[0:1]
	v_mad_u64_u32 v[2:3], s[40:41], v0, s93, v[2:3]
	v_mad_i32_i24 v3, v1, s93, v3
	s_mov_b64 s[40:41], 0x10a000
	v_lshl_add_u64 v[0:1], v[2:3], 0, s[40:41]
	s_branch .Lsti_10_1122
.Lsti_10_1122:
	s_or_b64 exec, exec, s[18:19]
.Lsti_10_1123:
	s_or_b64 exec, exec, s[14:15]
	v_mul_i32_i24_e32 v8, 0x200, v7
	v_lshlrev_b32_e32 v2, 2, v8
	v_sub_u32_e32 v2, v6, v2
	v_ashrrev_i32_e32 v3, 31, v2
	v_lshl_add_u64 v[0:1], v[2:3], 2, v[0:1]
	global_load_dwordx4 v[52:55], v[0:1], off
	v_lshlrev_b32_e32 v7, 12, v7
	v_add_u32_e32 v9, 0x200, v4
	v_cmp_lt_i32_e32 vcc, s26, v4
	v_lshlrev_b32_e32 v4, 3, v8
	v_sub_u32_e32 v4, v7, v4
	v_add_u32_e32 v66, v5, v4
	s_or_b64 s[12:13], vcc, s[12:13]
	v_add_u32_e32 v6, 0x800, v6
	v_add_u32_e32 v5, 0x1000, v5
	v_mov_b32_e32 v4, v9
	s_waitcnt vmcnt(10)
	v_cvt_pk_bf16_f32 v0, v12, v13
	v_cvt_pk_bf16_f32 v1, v14, v15
	ds_write_b64 v56, v[0:1]
	s_waitcnt vmcnt(9)
	v_cvt_pk_bf16_f32 v0, v16, v17
	v_cvt_pk_bf16_f32 v1, v18, v19
	ds_write_b64 v57, v[0:1]
	s_waitcnt vmcnt(8)
	v_cvt_pk_bf16_f32 v0, v20, v21
	v_cvt_pk_bf16_f32 v1, v22, v23
	ds_write_b64 v58, v[0:1]
	s_waitcnt vmcnt(7)
	v_cvt_pk_bf16_f32 v0, v24, v25
	v_cvt_pk_bf16_f32 v1, v26, v27
	ds_write_b64 v59, v[0:1]
	s_waitcnt vmcnt(6)
	v_cvt_pk_bf16_f32 v0, v28, v29
	v_cvt_pk_bf16_f32 v1, v30, v31
	ds_write_b64 v60, v[0:1]
	s_waitcnt vmcnt(5)
	v_cvt_pk_bf16_f32 v0, v32, v33
	v_cvt_pk_bf16_f32 v1, v34, v35
	ds_write_b64 v61, v[0:1]
	s_waitcnt vmcnt(4)
	v_cvt_pk_bf16_f32 v0, v36, v37
	v_cvt_pk_bf16_f32 v1, v38, v39
	ds_write_b64 v62, v[0:1]
	s_waitcnt vmcnt(3)
	v_cvt_pk_bf16_f32 v0, v40, v41
	v_cvt_pk_bf16_f32 v1, v42, v43
	ds_write_b64 v63, v[0:1]
	s_waitcnt vmcnt(2)
	v_cvt_pk_bf16_f32 v0, v44, v45
	v_cvt_pk_bf16_f32 v1, v46, v47
	ds_write_b64 v64, v[0:1]
	s_waitcnt vmcnt(1)
	v_cvt_pk_bf16_f32 v0, v48, v49
	v_cvt_pk_bf16_f32 v1, v50, v51
	ds_write_b64 v65, v[0:1]
	s_waitcnt vmcnt(0)
	v_cvt_pk_bf16_f32 v0, v52, v53
	v_cvt_pk_bf16_f32 v1, v54, v55
	ds_write_b64 v66, v[0:1]
